# adds: attention K/V tile prefetch addresses from scalar base + one constant per-lane offset (no 64-bit VALU multiply-adds per tile); uniform-branch test in the softmax rescale check shortened by two V
# speedup vs baseline: 1.0178x; 1.0085x over previous
.LBB0_783:
	s_and_b64 vcc, exec, s[0:1]
	s_cbranch_vccz .LBB0_762
	s_ashr_i32 s0, s16, 7
	s_lshl_b32 s18, s0, 11
	s_and_b32 s1, s17, 0x780
	s_or_b32 s17, s18, s1
	s_lshl_b32 s1, s16, 3
	s_and_b32 s1, s1, 0x380
	v_mbcnt_lo_u32_b32 v171, -1, 0
	v_mbcnt_hi_u32_b32 v171, -1, v171
	s_lshl_b32 s96, s1, 1
	v_lshlrev_b32_e32 v20, 3, v171
	v_and_b32_e32 v0, 0x78, v20
	s_add_u32 s20, s6, s96
	v_lshlrev_b32_e32 v16, 1, v0
	s_addc_u32 s21, s7, 0
	v_mov_b32_e32 v17, v113
	v_add_u32_e32 v172, s4, v171
	v_lshl_add_u64 v[166:167], s[20:21], 0, v[16:17]
	s_add_u32 s20, s8, s96
	v_ashrrev_i32_e32 v181, 4, v172
	s_addc_u32 s21, s9, 0
	v_lshl_add_u64 v[168:169], s[20:21], 0, v[16:17]
	v_mad_u32_u24 v241, v181, s62, v16
	v_add_u32_e32 v34, s18, v181
	v_mad_i64_i32 v[0:1], s[20:21], v34, s62, v[168:169]
	v_add_co_u32_e32 v4, vcc, s74, v0
	v_mad_i64_i32 v[8:9], s[20:21], v34, s62, v[166:167]
	s_nop 0
	v_addc_co_u32_e32 v5, vcc, 0, v1, vcc
	v_add_co_u32_e32 v12, vcc, s74, v8
	global_load_dwordx4 v[0:3], v[0:1], off
	s_nop 0
	global_load_dwordx4 v[4:7], v[4:5], off
	v_addc_co_u32_e32 v13, vcc, 0, v9, vcc
	global_load_dwordx4 v[8:11], v[8:9], off
	s_nop 0
	global_load_dwordx4 v[12:15], v[12:13], off
	v_lshrrev_b32_e32 v17, 1, v172
	v_and_b32_e32 v173, 31, v171
	v_and_b32_e32 v176, 0x60, v17
	v_mov_b64_e32 v[18:19], s[50:51]
	v_ashrrev_i32_e32 v175, 8, v172
	v_or3_b32 v29, v173, s17, v176
	v_bfe_u32 v22, v20, 5, 2
	v_lshlrev_b32_e32 v20, 6, v175
	v_mad_i64_i32 v[18:19], s[20:21], v29, s62, v[18:19]
	v_bfe_u32 v174, v171, 5, 1
	v_ashrrev_i32_e32 v21, 31, v20
	v_lshl_add_u64 v[18:19], v[18:19], 0, s[96:97]
	v_lshlrev_b32_e32 v112, 4, v174
	v_lshl_add_u64 v[18:19], v[20:21], 1, v[18:19]
	v_lshl_add_u64 v[18:19], v[18:19], 0, v[112:113]
	global_load_dwordx4 v[122:125], v[18:19], off
	global_load_dwordx4 v[126:129], v[18:19], off offset:32
	global_load_dwordx4 v[118:121], v[18:19], off offset:64
	global_load_dwordx4 v[114:117], v[18:19], off offset:96
	v_and_b32_e32 v17, 0xfffff0, v181
	v_lshlrev_b32_e32 v24, 1, v181
	v_add_u32_e32 v27, 32, v181
	v_lshrrev_b32_e32 v25, 1, v181
	v_and_b32_e32 v26, 3, v181
	v_and_or_b32 v17, v24, 8, v17
	v_and_b32_e32 v20, 0xfffff0, v27
	v_lshlrev_b32_e32 v21, 1, v27
	v_and_b32_e32 v23, 0x70, v172
	v_lshlrev_b32_e32 v28, 8, v181
	v_and_or_b32 v24, v25, 4, v26
	v_lshlrev_b32_e32 v26, 8, v27
	v_lshrrev_b32_e32 v17, 1, v17
	v_and_or_b32 v20, v21, 8, v20
	v_and_b32_e32 v25, 48, v16
	v_bitop3_b32 v182, v16, v28, v23 bitop3:0xde
	v_bitop3_b32 v183, v26, v16, v23 bitop3:0xf6
	v_and_b32_e32 v243, 16, v181
	v_lshlrev_b32_e32 v243, 3, v243
	v_xor_b32_e32 v182, v243, v182
	v_xor_b32_e32 v183, v243, v183
	v_or_b32_e32 v16, v17, v22
	v_lshrrev_b32_e32 v17, 1, v20
	v_lshlrev_b32_e32 v24, 6, v24
	v_lshlrev_b32_e32 v16, 9, v16
	v_or_b32_e32 v17, v17, v22
	v_or3_b32 v184, v16, v24, v25
	v_lshlrev_b32_e32 v16, 9, v17
	v_or3_b32 v185, v16, v24, v25
	v_add_u32_e32 v32, 0, v184
	v_add_u32_e32 v21, 0, v182
	v_add_u32_e32 v20, 0, v183
	v_add_u32_e32 v33, 0, v185
	s_waitcnt vmcnt(0)
	v_lshlrev_b32_e32 v38, 7, v175
	v_lshlrev_b32_e32 v189, 8, v173
	v_add_u32_e32 v191, 0, v189
	s_movk_i32 s1, 0x60
	s_waitcnt vmcnt(7)
	ds_write_b128 v32, v[0:3] offset:1024
	s_waitcnt vmcnt(6)
	ds_write_b128 v33, v[4:7] offset:1024
	s_waitcnt vmcnt(5)
	ds_write_b128 v21, v[8:11] offset:50176
	s_waitcnt vmcnt(4)
	ds_write_b128 v20, v[12:15] offset:50176
	v_add_u32_e32 v4, 64, v34
	v_mad_i64_i32 v[0:1], s[20:21], v4, s62, v[168:169]
	v_add_co_u32_e32 v2, vcc, s74, v0
	s_nop 1
	v_addc_co_u32_e32 v3, vcc, 0, v1, vcc
	global_load_dwordx4 v[16:19], v[0:1], off
	global_load_dwordx4 v[20:23], v[2:3], off
	v_mad_i64_i32 v[0:1], s[20:21], v4, s62, v[166:167]
	v_add_co_u32_e32 v2, vcc, s74, v0
	v_add_u32_e32 v4, 0x80, v34
	s_nop 0
	v_addc_co_u32_e32 v3, vcc, 0, v1, vcc
	global_load_dwordx4 v[24:27], v[0:1], off
	global_load_dwordx4 v[28:31], v[2:3], off
	v_mad_i64_i32 v[0:1], s[20:21], v4, s62, v[166:167]
	v_add_co_u32_e32 v2, vcc, s74, v0
	s_nop 1
	v_addc_co_u32_e32 v3, vcc, 0, v1, vcc
	global_load_dwordx4 v[142:145], v[2:3], off
	global_load_dwordx4 v[138:141], v[0:1], off
	v_mad_i64_i32 v[0:1], s[20:21], v4, s62, v[168:169]
	v_add_co_u32_e32 v2, vcc, s74, v0
	s_nop 1
	v_addc_co_u32_e32 v3, vcc, 0, v1, vcc
	global_load_dwordx4 v[134:137], v[2:3], off
	global_load_dwordx4 v[130:133], v[0:1], off
	v_lshlrev_b32_e32 v0, 4, v171
	v_and_b32_e32 v39, 0x70, v0
	v_bitop3_b32 v190, v38, v39, v112 bitop3:0x36
	v_and_b32_e32 v244, 16, v171
	v_lshlrev_b32_e32 v244, 3, v244
	v_xor_b32_e32 v190, v244, v190
	v_add_u32_e32 v34, v191, v190
	s_waitcnt lgkmcnt(0)
	s_barrier
	ds_read_b128 v[0:3], v34 offset:50176
	ds_read_b128 v[34:37], v34 offset:58368
	v_or_b32_e32 v38, v38, v112
	v_bitop3_b32 v188, v38, v39, 32 bitop3:0x36
	v_xor_b32_e32 v188, v244, v188
	v_add_u32_e32 v40, v191, v188
	s_waitcnt vmcnt(11) lgkmcnt(0)
	v_mfma_f32_32x32x16_bf16 v[64:79], v[34:37], v[122:125], 0
	ds_read_b128 v[34:37], v40 offset:50176
	v_bitop3_b32 v187, v38, v39, 64 bitop3:0x36
	v_bitop3_b32 v186, v38, v39, s1 bitop3:0x36
	v_xor_b32_e32 v187, v244, v187
	v_xor_b32_e32 v186, v244, v186
	v_add_u32_e32 v38, v191, v186
	v_mfma_f32_32x32x16_bf16 v[0:15], v[0:3], v[122:125], 0
	s_waitcnt vmcnt(10) lgkmcnt(0)
	v_mfma_f32_32x32x16_bf16 v[0:15], v[34:37], v[126:129], v[0:15]
	ds_read_b128 v[34:37], v40 offset:58368
	v_add_u32_e32 v40, v191, v187
	s_waitcnt lgkmcnt(0)
	v_mfma_f32_32x32x16_bf16 v[64:79], v[34:37], v[126:129], v[64:79]
	ds_read_b128 v[34:37], v40 offset:50176
	s_waitcnt vmcnt(9) lgkmcnt(0)
	v_mfma_f32_32x32x16_bf16 v[0:15], v[34:37], v[118:121], v[0:15]
	ds_read_b128 v[34:37], v40 offset:58368
	s_waitcnt lgkmcnt(0)
	v_mfma_f32_32x32x16_bf16 v[64:79], v[34:37], v[118:121], v[64:79]
	ds_read_b128 v[34:37], v38 offset:50176
	s_waitcnt vmcnt(8) lgkmcnt(0)
	v_mfma_f32_32x32x16_bf16 v[0:15], v[34:37], v[114:117], v[0:15]
	ds_read_b128 v[34:37], v38 offset:58368
	s_waitcnt lgkmcnt(0)
	v_mfma_f32_32x32x16_bf16 v[64:79], v[34:37], v[114:117], v[64:79]
	s_nop 8
	v_max_f32_e32 v34, v1, v1
	v_max_f32_e32 v35, v0, v0
	v_max_f32_e32 v34, v35, v34
	v_max3_f32 v34, v34, v2, v3
	v_max3_f32 v34, v34, v4, v5
	v_max3_f32 v34, v34, v6, v7
	v_max3_f32 v34, v34, v8, v9
	v_max3_f32 v34, v34, v10, v11
	v_max3_f32 v34, v34, v12, v13
	v_max3_f32 v34, v34, v14, v15
	v_max3_f32 v34, v34, v64, v65
	v_max3_f32 v34, v34, v66, v67
	v_max3_f32 v34, v34, v68, v69
	v_max3_f32 v34, v34, v70, v71
	v_max3_f32 v34, v34, v72, v73
	v_max3_f32 v34, v34, v74, v75
	v_max3_f32 v34, v34, v76, v77
	v_max3_f32 v34, v34, v78, v79
	v_mov_b32_e32 v35, v34
	s_nop 1
	v_permlane32_swap_b32_e32 v34, v35
	v_max_f32_e32 v35, v35, v35
	v_max_f32_e32 v34, v34, v34
	v_max_f32_e32 v34, v34, v35
	v_cmp_ge_f32_e32 vcc, s75, v34
	s_cmp_eq_u64 vcc, exec
	s_cbranch_scc0 .LBB0_814
	v_mov_b32_e32 v193, 1.0
	v_mov_b32_e32 v164, 0

.LBB0_787:
	s_mov_b32 s54, s0
	s_add_i32 s55, s28, -3
	s_lshl_b32 s21, s0, 14
	v_add_u32_e32 v180, s21, v191
	v_add_u32_e32 v84, v180, v190
	ds_read_b128 v[80:83], v84 offset:50176
	ds_read_b128 v[84:87], v84 offset:58368
	v_add_u32_e32 v195, v180, v188
	ds_read_b128 v[196:199], v195 offset:50176
	ds_read_b128 v[200:203], v195 offset:58368
	v_add_u32_e32 v195, v180, v187
	s_waitcnt lgkmcnt(3)
	v_mfma_f32_32x32x16_bf16 v[96:111], v[80:83], v[122:125], 0
	v_add_u32_e32 v180, v180, v186
	v_exp_f32_e32 v204, v72
	v_exp_f32_e32 v205, v73
	v_exp_f32_e32 v206, v74
	v_exp_f32_e32 v207, v75
	v_exp_f32_e32 v208, v76
	v_exp_f32_e32 v209, v77
	s_waitcnt lgkmcnt(2)
	v_mfma_f32_32x32x16_bf16 v[80:95], v[84:87], v[122:125], 0
	v_exp_f32_e32 v210, v78
	v_exp_f32_e32 v79, v79
	s_waitcnt lgkmcnt(1)
	v_mfma_f32_32x32x16_bf16 v[96:111], v[196:199], v[126:129], v[96:111]
	s_waitcnt lgkmcnt(0)
	v_mfma_f32_32x32x16_bf16 v[80:95], v[200:203], v[126:129], v[80:95]
	ds_read_b128 v[196:199], v195 offset:50176
	ds_read_b128 v[200:203], v195 offset:58368
	s_waitcnt lgkmcnt(1)
	v_mfma_f32_32x32x16_bf16 v[96:111], v[196:199], v[118:121], v[96:111]
	s_waitcnt lgkmcnt(0)
	v_mfma_f32_32x32x16_bf16 v[80:95], v[200:203], v[118:121], v[80:95]
	ds_read_b128 v[196:199], v180 offset:50176
	ds_read_b128 v[200:203], v180 offset:58368
	v_exp_f32_e32 v180, v64
	v_add_f32_e32 v64, 0, v159
	v_add_f32_e32 v64, v161, v64
	v_add_f32_e32 v64, v157, v64
	v_add_f32_e32 v64, v160, v64
	v_add_f32_e32 v64, v155, v64
	v_add_f32_e32 v64, v158, v64
	v_add_f32_e32 v64, v154, v64
	v_add_f32_e32 v64, v156, v64
	v_add_f32_e32 v64, v151, v64
	v_add_f32_e32 v64, v153, v64
	v_add_f32_e32 v64, v149, v64
	v_add_f32_e32 v64, v152, v64
	v_add_f32_e32 v64, v147, v64
	s_waitcnt lgkmcnt(1)
	v_mfma_f32_32x32x16_bf16 v[96:111], v[196:199], v[114:117], v[96:111]
	v_exp_f32_e32 v197, v65
	v_add_f32_e32 v64, v150, v64
	v_exp_f32_e32 v198, v66
	v_add_f32_e32 v64, v146, v64
	v_exp_f32_e32 v199, v67
	v_add_f32_e32 v64, v148, v64
	v_add_f32_e32 v64, v180, v64
	s_waitcnt lgkmcnt(0)
	v_mfma_f32_32x32x16_bf16 v[80:95], v[200:203], v[114:117], v[80:95]
	v_exp_f32_e32 v200, v68
	v_exp_f32_e32 v201, v69
	v_add_f32_e32 v64, v197, v64
	v_exp_f32_e32 v202, v70
	v_add_f32_e32 v64, v198, v64
	v_exp_f32_e32 v203, v71
	v_add_f32_e32 v64, v199, v64
	v_add_f32_e32 v64, v200, v64
	v_add_f32_e32 v64, v201, v64
	v_add_f32_e32 v64, v202, v64
	v_add_f32_e32 v64, v203, v64
	v_add_f32_e32 v64, v204, v64
	v_add_f32_e32 v64, v205, v64
	v_add_f32_e32 v64, v206, v64
	v_add_f32_e32 v64, v207, v64
	v_add_f32_e32 v64, v208, v64
	v_add_f32_e32 v64, v209, v64
	v_add_f32_e32 v64, v210, v64
	v_add_f32_e32 v195, v79, v64
	v_mov_b32_e32 v196, v195
	v_cvt_pk_bf16_f32 v64, v159, v161
	v_cvt_pk_bf16_f32 v65, v157, v160
	v_cvt_pk_bf16_f32 v66, v155, v158
	s_nop 1
	v_permlane32_swap_b32_e32 v195, v196
	v_cvt_pk_bf16_f32 v67, v154, v156
	v_permlane32_swap_b32_e32 v64, v66
	v_cvt_pk_bf16_f32 v68, v151, v153
	v_cvt_pk_bf16_f32 v69, v149, v152
	v_cvt_pk_bf16_f32 v70, v147, v150
	v_cvt_pk_bf16_f32 v71, v146, v148
	v_cvt_pk_bf16_f32 v72, v180, v197
	v_cvt_pk_bf16_f32 v73, v198, v199
	v_cvt_pk_bf16_f32 v74, v200, v201
	v_cvt_pk_bf16_f32 v75, v202, v203
	v_cvt_pk_bf16_f32 v76, v204, v205
	v_cvt_pk_bf16_f32 v77, v206, v207
	v_cvt_pk_bf16_f32 v78, v208, v209
	v_cvt_pk_bf16_f32 v79, v210, v79
	v_permlane32_swap_b32_e32 v65, v67
	v_permlane32_swap_b32_e32 v68, v70
	v_permlane32_swap_b32_e32 v69, v71
	v_permlane32_swap_b32_e32 v72, v74
	v_permlane32_swap_b32_e32 v73, v75
	v_permlane32_swap_b32_e32 v76, v78
	v_permlane32_swap_b32_e32 v77, v79
	s_cmp_lt_u32 s55, 30
	s_cselect_b32 s0, 0, 0xffffffe0
	s_cselect_b32 s1, s18, s16
	s_add_i32 s0, s0, s28
	s_lshl_b32 s0, s0, 6
	s_add_i32 s0, s0, s1
	s_sub_i32 s0, s0, 64
	s_mul_i32 s64, s0, 0x1800
	s_add_u32 s66, s8, s96
	s_addc_u32 s67, s9, 0
	s_add_u32 s66, s66, s64
	s_addc_u32 s67, s67, 0
	s_add_u32 s68, s66, 0x30000
	s_addc_u32 s69, s67, 0
	s_add_u32 s70, s6, s96
	s_addc_u32 s71, s7, 0
	s_add_u32 s70, s70, s64
	s_addc_u32 s71, s71, 0
	s_add_u32 s72, s70, 0x30000
	s_addc_u32 s73, s71, 0
	global_load_dwordx4 v[146:149], v241, s[66:67]
	global_load_dwordx4 v[150:153], v241, s[68:69]
	global_load_dwordx4 v[154:157], v241, s[70:71]
	global_load_dwordx4 v[158:161], v241, s[72:73]
	s_lshl_b32 s20, s29, 14
	v_add_u32_e32 v180, s20, v194
	ds_read_b64_tr_b16 v[198:199], v180 offset:0
	ds_read_b64_tr_b16 v[200:201], v180 offset:0x800
	ds_read_b64_tr_b16 v[202:203], v180 offset:0x1000
	ds_read_b64_tr_b16 v[204:205], v180 offset:0x1800
	ds_read_b64_tr_b16 v[206:207], v180 offset:0x2000
	ds_read_b64_tr_b16 v[208:209], v180 offset:0x2800
	ds_read_b64_tr_b16 v[222:223], v180 offset:0x3000
	ds_read_b64_tr_b16 v[224:225], v180 offset:0x3800
	s_waitcnt lgkmcnt(0)
	s_nop 0
	v_mfma_f32_32x32x16_bf16 v[0:15], v[64:67], v[198:201], v[0:15]
	ds_read_b64_tr_b16 v[198:199], v180 offset:0x200
	ds_read_b64_tr_b16 v[200:201], v180 offset:0xa00
	v_mfma_f32_32x32x16_bf16 v[0:15], v[68:71], v[202:205], v[0:15]
	ds_read_b64_tr_b16 v[202:203], v180 offset:0x1200
	ds_read_b64_tr_b16 v[204:205], v180 offset:0x1a00
	v_mfma_f32_32x32x16_bf16 v[0:15], v[72:75], v[206:209], v[0:15]
	ds_read_b64_tr_b16 v[206:207], v180 offset:0x2200
	ds_read_b64_tr_b16 v[208:209], v180 offset:0x2a00
	v_mfma_f32_32x32x16_bf16 v[0:15], v[76:79], v[222:225], v[0:15]
	ds_read_b64_tr_b16 v[222:223], v180 offset:0x3200
	ds_read_b64_tr_b16 v[224:225], v180 offset:0x3a00
	s_waitcnt lgkmcnt(0)
	v_mfma_f32_32x32x16_bf16 v[48:63], v[64:67], v[198:201], v[48:63]
	ds_read_b64_tr_b16 v[198:199], v180 offset:0x400
	ds_read_b64_tr_b16 v[200:201], v180 offset:0xc00
	v_mfma_f32_32x32x16_bf16 v[48:63], v[68:71], v[202:205], v[48:63]
	ds_read_b64_tr_b16 v[202:203], v180 offset:0x1400
	ds_read_b64_tr_b16 v[204:205], v180 offset:0x1c00
	v_mfma_f32_32x32x16_bf16 v[48:63], v[72:75], v[206:209], v[48:63]
	ds_read_b64_tr_b16 v[206:207], v180 offset:0x2400
	ds_read_b64_tr_b16 v[208:209], v180 offset:0x2c00
	v_mfma_f32_32x32x16_bf16 v[48:63], v[76:79], v[222:225], v[48:63]
	ds_read_b64_tr_b16 v[222:223], v180 offset:0x3400
	ds_read_b64_tr_b16 v[224:225], v180 offset:0x3c00
	s_waitcnt lgkmcnt(0)
	v_mfma_f32_32x32x16_bf16 v[32:47], v[64:67], v[198:201], v[32:47]
	ds_read_b64_tr_b16 v[198:199], v180 offset:0x600
	ds_read_b64_tr_b16 v[200:201], v180 offset:0xe00
	v_mfma_f32_32x32x16_bf16 v[32:47], v[68:71], v[202:205], v[32:47]
	ds_read_b64_tr_b16 v[202:203], v180 offset:0x1600
	ds_read_b64_tr_b16 v[204:205], v180 offset:0x1e00
	v_mfma_f32_32x32x16_bf16 v[32:47], v[72:75], v[206:209], v[32:47]
	ds_read_b64_tr_b16 v[206:207], v180 offset:0x2600
	ds_read_b64_tr_b16 v[208:209], v180 offset:0x2e00
	v_mfma_f32_32x32x16_bf16 v[32:47], v[76:79], v[222:225], v[32:47]
	ds_read_b64_tr_b16 v[222:223], v180 offset:0x3600
	ds_read_b64_tr_b16 v[224:225], v180 offset:0x3e00
	s_waitcnt lgkmcnt(0)
	v_mfma_f32_32x32x16_bf16 v[16:31], v[64:67], v[198:201], v[16:31]
	v_max_f32_e32 v64, v97, v97
	v_max_f32_e32 v65, v96, v96
	v_max_f32_e32 v64, v65, v64
	v_max3_f32 v64, v64, v98, v99
	v_max3_f32 v64, v64, v100, v101
	v_max3_f32 v64, v64, v102, v103
	v_max3_f32 v64, v64, v104, v105
	v_mfma_f32_32x32x16_bf16 v[16:31], v[68:71], v[202:205], v[16:31]
	v_max3_f32 v64, v64, v106, v107
	v_max3_f32 v64, v64, v108, v109
	v_max3_f32 v64, v64, v110, v111
	v_max3_f32 v64, v64, v80, v81
	v_max3_f32 v64, v64, v82, v83
	v_max3_f32 v64, v64, v84, v85
	v_max3_f32 v64, v64, v86, v87
	v_mfma_f32_32x32x16_bf16 v[16:31], v[72:75], v[206:209], v[16:31]
	v_max3_f32 v64, v64, v88, v89
	v_max3_f32 v64, v64, v90, v91
	v_max3_f32 v64, v64, v92, v93
	v_max3_f32 v64, v64, v94, v95
	v_mov_b32_e32 v65, v64
	s_nop 1
	v_permlane32_swap_b32_e32 v64, v65
	v_mfma_f32_32x32x16_bf16 v[16:31], v[76:79], v[222:225], v[16:31]
	v_max_f32_e32 v65, v65, v65
	v_max_f32_e32 v64, v64, v64
	v_max_f32_e32 v64, v64, v65
	v_cmp_eq_f32_e32 vcc, 0, v164
	v_cmp_ge_f32_e64 s[40:41], s75, v64
	s_and_b64 s[0:1], vcc, s[40:41]
	s_cmp_eq_u64 s[0:1], exec
	v_mov_b32_e32 v198, 1.0
	s_cbranch_scc0 .LBB0_801

.LBB0_792:
	v_exp_f32_e32 v197, v96
	v_exp_f32_e32 v208, v97
	v_exp_f32_e32 v209, v98
	v_exp_f32_e32 v210, v99
	v_exp_f32_e32 v211, v100
	v_exp_f32_e32 v220, v101
	v_exp_f32_e32 v221, v102
	v_exp_f32_e32 v222, v103
	v_exp_f32_e32 v223, v104
	v_exp_f32_e32 v224, v105
	v_exp_f32_e32 v225, v106
	v_exp_f32_e32 v226, v107
	v_exp_f32_e32 v227, v108
	v_exp_f32_e32 v228, v109
	v_exp_f32_e32 v229, v110
	v_exp_f32_e32 v230, v111
	s_waitcnt lgkmcnt(0)
	s_barrier
	v_add_u32_e32 v199, s22, v189
	v_add_u32_e32 v68, v199, v190
	ds_read_b128 v[64:67], v68 offset:50176
	ds_read_b128 v[68:71], v68 offset:58368
	v_add_u32_e32 v204, v199, v188
	ds_read_b128 v[200:203], v204 offset:50176
	ds_read_b128 v[204:207], v204 offset:58368
	v_exp_f32_e32 v231, v87
	s_waitcnt lgkmcnt(3)
	v_mfma_f32_32x32x16_bf16 v[96:111], v[64:67], v[122:125], 0
	v_exp_f32_e32 v232, v88
	v_exp_f32_e32 v233, v89
	v_exp_f32_e32 v234, v90
	v_exp_f32_e32 v235, v91
	v_exp_f32_e32 v236, v92
	v_exp_f32_e32 v237, v93
	v_exp_f32_e32 v238, v94
	s_waitcnt lgkmcnt(2)
	v_mfma_f32_32x32x16_bf16 v[64:79], v[68:71], v[122:125], 0
	v_exp_f32_e32 v95, v95
	s_waitcnt lgkmcnt(1)
	v_mfma_f32_32x32x16_bf16 v[96:111], v[200:203], v[126:129], v[96:111]
	s_waitcnt lgkmcnt(0)
	v_mfma_f32_32x32x16_bf16 v[64:79], v[204:207], v[126:129], v[64:79]
	v_add_u32_e32 v204, v199, v187
	ds_read_b128 v[200:203], v204 offset:50176
	ds_read_b128 v[204:207], v204 offset:58368
	v_add_u32_e32 v199, v199, v186
	s_waitcnt lgkmcnt(1)
	v_mfma_f32_32x32x16_bf16 v[96:111], v[200:203], v[118:121], v[96:111]
	s_waitcnt lgkmcnt(0)
	v_mfma_f32_32x32x16_bf16 v[64:79], v[204:207], v[118:121], v[64:79]
	ds_read_b128 v[200:203], v199 offset:50176
	ds_read_b128 v[204:207], v199 offset:58368
	s_waitcnt lgkmcnt(1)
	v_mfma_f32_32x32x16_bf16 v[96:111], v[200:203], v[114:117], v[96:111]
	v_exp_f32_e32 v201, v80
	v_add_f32_e32 v80, 0, v197
	v_add_f32_e32 v80, v208, v80
	v_add_f32_e32 v80, v209, v80
	v_add_f32_e32 v80, v210, v80
	v_add_f32_e32 v80, v211, v80
	v_add_f32_e32 v80, v220, v80
	v_add_f32_e32 v80, v221, v80
	v_add_f32_e32 v80, v222, v80
	v_add_f32_e32 v80, v223, v80
	v_add_f32_e32 v80, v224, v80
	v_add_f32_e32 v80, v225, v80
	v_add_f32_e32 v80, v226, v80
	v_add_f32_e32 v80, v227, v80
	v_exp_f32_e32 v202, v81
	v_add_f32_e32 v80, v228, v80
	v_exp_f32_e32 v203, v82
	v_add_f32_e32 v80, v229, v80
	s_waitcnt lgkmcnt(0)
	v_mfma_f32_32x32x16_bf16 v[64:79], v[204:207], v[114:117], v[64:79]
	v_exp_f32_e32 v204, v83
	v_add_f32_e32 v80, v230, v80
	v_exp_f32_e32 v205, v84
	v_add_f32_e32 v80, v201, v80
	v_exp_f32_e32 v206, v85
	v_add_f32_e32 v80, v202, v80
	v_exp_f32_e32 v207, v86
	v_add_f32_e32 v80, v203, v80
	v_add_f32_e32 v80, v204, v80
	v_add_f32_e32 v80, v205, v80
	v_add_f32_e32 v80, v206, v80
	v_add_f32_e32 v80, v207, v80
	v_add_f32_e32 v80, v231, v80
	v_add_f32_e32 v80, v232, v80
	v_add_f32_e32 v80, v233, v80
	v_add_f32_e32 v80, v234, v80
	v_add_f32_e32 v80, v235, v80
	v_add_f32_e32 v80, v236, v80
	v_add_f32_e32 v80, v237, v80
	v_add_f32_e32 v80, v238, v80
	v_add_f32_e32 v199, v95, v80
	v_mov_b32_e32 v200, v199
	v_cvt_pk_bf16_f32 v80, v197, v208
	v_cvt_pk_bf16_f32 v81, v209, v210
	v_cvt_pk_bf16_f32 v82, v211, v220
	v_cvt_pk_bf16_f32 v83, v221, v222
	v_cvt_pk_bf16_f32 v84, v223, v224
	v_cvt_pk_bf16_f32 v85, v225, v226
	v_cvt_pk_bf16_f32 v86, v227, v228
	v_cvt_pk_bf16_f32 v87, v229, v230
	v_cvt_pk_bf16_f32 v88, v201, v202
	v_cvt_pk_bf16_f32 v89, v203, v204
	v_cvt_pk_bf16_f32 v90, v205, v206
	v_cvt_pk_bf16_f32 v91, v207, v231
	v_cvt_pk_bf16_f32 v92, v232, v233
	v_cvt_pk_bf16_f32 v93, v234, v235
	v_cvt_pk_bf16_f32 v94, v236, v237
	v_cvt_pk_bf16_f32 v95, v238, v95
	s_nop 1
	v_permlane32_swap_b32_e32 v199, v200
	v_permlane32_swap_b32_e32 v80, v82
	v_permlane32_swap_b32_e32 v81, v83
	v_permlane32_swap_b32_e32 v84, v86
	v_permlane32_swap_b32_e32 v85, v87
	v_permlane32_swap_b32_e32 v88, v90
	v_permlane32_swap_b32_e32 v89, v91
	v_permlane32_swap_b32_e32 v92, v94
	v_permlane32_swap_b32_e32 v93, v95
	s_cmp_gt_u32 s55, 32
	s_cbranch_scc1 .LBB0_794
	s_cmp_lt_u32 s55, 29
	s_cselect_b32 s0, 0, 0xffffffe0
	s_cselect_b32 s1, s18, s16
	s_add_i32 s0, s0, s28
	s_lshl_b32 s0, s0, 6
	s_add_i32 s0, s0, s1
	s_mul_i32 s64, s0, 0x1800
	s_add_u32 s66, s8, s96
	s_addc_u32 s67, s9, 0
	s_add_u32 s66, s66, s64
	s_addc_u32 s67, s67, 0
	s_add_u32 s68, s66, 0x30000
	s_addc_u32 s69, s67, 0
	s_add_u32 s70, s6, s96
	s_addc_u32 s71, s7, 0
	s_add_u32 s70, s70, s64
	s_addc_u32 s71, s71, 0
	s_add_u32 s72, s70, 0x30000
	s_addc_u32 s73, s71, 0
	global_load_dwordx4 v[130:133], v241, s[66:67]
	global_load_dwordx4 v[134:137], v241, s[68:69]
	global_load_dwordx4 v[138:141], v241, s[70:71]
	global_load_dwordx4 v[142:145], v241, s[72:73]
.LBB0_794:
	v_add_u32_e32 v197, s21, v194
	ds_read_b64_tr_b16 v[202:203], v197 offset:0
	ds_read_b64_tr_b16 v[204:205], v197 offset:0x800
	ds_read_b64_tr_b16 v[206:207], v197 offset:0x1000
	ds_read_b64_tr_b16 v[208:209], v197 offset:0x1800
	ds_read_b64_tr_b16 v[222:223], v197 offset:0x2000
	ds_read_b64_tr_b16 v[224:225], v197 offset:0x2800
	ds_read_b64_tr_b16 v[226:227], v197 offset:0x3000
	ds_read_b64_tr_b16 v[228:229], v197 offset:0x3800
	s_waitcnt lgkmcnt(0)
	s_nop 0
	v_mfma_f32_32x32x16_bf16 v[0:15], v[80:83], v[202:205], v[0:15]
	ds_read_b64_tr_b16 v[202:203], v197 offset:0x200
	ds_read_b64_tr_b16 v[204:205], v197 offset:0xa00
	v_mfma_f32_32x32x16_bf16 v[0:15], v[84:87], v[206:209], v[0:15]
	ds_read_b64_tr_b16 v[206:207], v197 offset:0x1200
	ds_read_b64_tr_b16 v[208:209], v197 offset:0x1a00
	v_mfma_f32_32x32x16_bf16 v[0:15], v[88:91], v[222:225], v[0:15]
	ds_read_b64_tr_b16 v[222:223], v197 offset:0x2200
	ds_read_b64_tr_b16 v[224:225], v197 offset:0x2a00
	v_mfma_f32_32x32x16_bf16 v[0:15], v[92:95], v[226:229], v[0:15]
	ds_read_b64_tr_b16 v[226:227], v197 offset:0x3200
	ds_read_b64_tr_b16 v[228:229], v197 offset:0x3a00
	s_waitcnt lgkmcnt(0)
	v_mfma_f32_32x32x16_bf16 v[48:63], v[80:83], v[202:205], v[48:63]
	ds_read_b64_tr_b16 v[202:203], v197 offset:0x400
	ds_read_b64_tr_b16 v[204:205], v197 offset:0xc00
	v_mfma_f32_32x32x16_bf16 v[48:63], v[84:87], v[206:209], v[48:63]
	ds_read_b64_tr_b16 v[206:207], v197 offset:0x1400
	ds_read_b64_tr_b16 v[208:209], v197 offset:0x1c00
	v_mfma_f32_32x32x16_bf16 v[48:63], v[88:91], v[222:225], v[48:63]
	ds_read_b64_tr_b16 v[222:223], v197 offset:0x2400
	ds_read_b64_tr_b16 v[224:225], v197 offset:0x2c00
	v_mfma_f32_32x32x16_bf16 v[48:63], v[92:95], v[226:229], v[48:63]
	ds_read_b64_tr_b16 v[226:227], v197 offset:0x3400
	ds_read_b64_tr_b16 v[228:229], v197 offset:0x3c00
	s_waitcnt lgkmcnt(0)
	v_mfma_f32_32x32x16_bf16 v[32:47], v[80:83], v[202:205], v[32:47]
	ds_read_b64_tr_b16 v[202:203], v197 offset:0x600
	ds_read_b64_tr_b16 v[204:205], v197 offset:0xe00
	v_mfma_f32_32x32x16_bf16 v[32:47], v[84:87], v[206:209], v[32:47]
	ds_read_b64_tr_b16 v[206:207], v197 offset:0x1600
	ds_read_b64_tr_b16 v[208:209], v197 offset:0x1e00
	v_mfma_f32_32x32x16_bf16 v[32:47], v[88:91], v[222:225], v[32:47]
	ds_read_b64_tr_b16 v[222:223], v197 offset:0x2600
	ds_read_b64_tr_b16 v[224:225], v197 offset:0x2e00
	v_mfma_f32_32x32x16_bf16 v[32:47], v[92:95], v[226:229], v[32:47]
	ds_read_b64_tr_b16 v[226:227], v197 offset:0x3600
	ds_read_b64_tr_b16 v[228:229], v197 offset:0x3e00
	s_waitcnt lgkmcnt(0)
	v_mfma_f32_32x32x16_bf16 v[16:31], v[80:83], v[202:205], v[16:31]
	v_max_f32_e32 v80, v97, v97
	v_max_f32_e32 v81, v96, v96
	v_max_f32_e32 v80, v81, v80
	v_max3_f32 v80, v80, v98, v99
	v_max3_f32 v80, v80, v100, v101
	v_max3_f32 v80, v80, v102, v103
	v_max3_f32 v80, v80, v104, v105
	v_mfma_f32_32x32x16_bf16 v[16:31], v[84:87], v[206:209], v[16:31]
	v_max3_f32 v80, v80, v106, v107
	v_max3_f32 v80, v80, v108, v109
	v_max3_f32 v80, v80, v110, v111
	v_max3_f32 v80, v80, v64, v65
	v_max3_f32 v80, v80, v66, v67
	v_max3_f32 v80, v80, v68, v69
	v_max3_f32 v80, v80, v70, v71
	v_mfma_f32_32x32x16_bf16 v[16:31], v[88:91], v[222:225], v[16:31]
	v_max3_f32 v80, v80, v72, v73
	v_max3_f32 v80, v80, v74, v75
	v_max3_f32 v80, v80, v76, v77
	v_max3_f32 v80, v80, v78, v79
	v_mov_b32_e32 v81, v80
	s_nop 1
	v_permlane32_swap_b32_e32 v80, v81
	v_mfma_f32_32x32x16_bf16 v[16:31], v[92:95], v[226:229], v[16:31]
	v_max_f32_e32 v81, v81, v81
	v_max_f32_e32 v80, v80, v80
	v_max_f32_e32 v80, v80, v81
	v_cmp_eq_f32_e32 vcc, 0, v164
	v_cmp_ge_f32_e64 s[40:41], s75, v80
	s_and_b64 s[0:1], vcc, s[40:41]
	s_cmp_eq_u64 s[0:1], exec
	v_mov_b32_e32 v197, 1.0
	s_cbranch_scc0 .LBB0_802
